# grid barrier: non-last workgroups poll the top generation word directly (one release hop fewer), XCD-last no longer bumps per-XCD gen; dropped redundant 32-state nop pad before fp8 epilogues
# speedup vs baseline: 1.0136x; 1.0030x over previous
.LBB0_274:
	s_or_b64 exec, exec, s[4:5]
	s_waitcnt vmcnt(0)
	buffer_inv sc1
	s_waitcnt vmcnt(0)

.LBB0_391:
	s_lshl_b32 s0, s0, 8
	s_and_b32 vcc_lo, s4, -2
	s_cmp_eq_u32 vcc_lo, 6
	s_cbranch_scc1 .Lepi_old_ip8
	s_cmp_gt_i32 s4, 14
	s_cbranch_scc1 .Lepi_gate_ip8
	v_mbcnt_lo_u32_b32 v2, -1, 0
	v_mbcnt_hi_u32_b32 v2, -1, v2
	s_add_i32 s0, s0, s81
	v_and_or_b32 v8, v2, 15, s0
	v_ashrrev_i32_e32 v2, 1, v2
	s_lshl_b32 s0, s4, 8
	v_and_b32_e32 v2, -8, v2
	s_or_b32 s0, s0, s6
	v_add_u32_e32 v2, s0, v2
	v_mov_b64_e32 v[4:5], s[8:9]
	v_ashrrev_i32_e32 v3, 31, v2
	v_mad_i64_i32 v[6:7], vcc, v8, s88, v[4:5]
	v_lshl_add_u64 v[6:7], v[2:3], 1, v[6:7]
	v_cvt_pk_bf16_f32 v10, v158, v159
	v_cvt_pk_bf16_f32 v11, v160, v161
	v_cvt_pk_bf16_f32 v12, v154, v155
	v_cvt_pk_bf16_f32 v13, v156, v157
	global_store_dwordx4 v[6:7], v[10:13], off
	v_cvt_pk_bf16_f32 v14, v126, v127
	v_cvt_pk_bf16_f32 v15, v128, v129
	v_cvt_pk_bf16_f32 v16, v122, v123
	v_cvt_pk_bf16_f32 v17, v124, v125
	global_store_dwordx4 v[6:7], v[14:17], off offset:256
	v_add_u32_e32 v9, 16, v8
	v_mad_i64_i32 v[6:7], vcc, v9, s88, v[4:5]
	v_lshl_add_u64 v[6:7], v[2:3], 1, v[6:7]
	v_cvt_pk_bf16_f32 v10, v150, v151
	v_cvt_pk_bf16_f32 v11, v152, v153
	v_cvt_pk_bf16_f32 v12, v146, v147
	v_cvt_pk_bf16_f32 v13, v148, v149
	global_store_dwordx4 v[6:7], v[10:13], off
	v_cvt_pk_bf16_f32 v14, v118, v119
	v_cvt_pk_bf16_f32 v15, v120, v121
	v_cvt_pk_bf16_f32 v16, v114, v115
	v_cvt_pk_bf16_f32 v17, v116, v117
	global_store_dwordx4 v[6:7], v[14:17], off offset:256
	v_add_u32_e32 v9, 32, v8
	v_mad_i64_i32 v[6:7], vcc, v9, s88, v[4:5]
	v_lshl_add_u64 v[6:7], v[2:3], 1, v[6:7]
	v_cvt_pk_bf16_f32 v10, v142, v143
	v_cvt_pk_bf16_f32 v11, v144, v145
	v_cvt_pk_bf16_f32 v12, v138, v139
	v_cvt_pk_bf16_f32 v13, v140, v141
	global_store_dwordx4 v[6:7], v[10:13], off
	v_cvt_pk_bf16_f32 v14, v110, v111
	v_cvt_pk_bf16_f32 v15, v112, v113
	v_cvt_pk_bf16_f32 v16, v106, v107
	v_cvt_pk_bf16_f32 v17, v108, v109
	global_store_dwordx4 v[6:7], v[14:17], off offset:256
	v_add_u32_e32 v9, 48, v8
	v_mad_i64_i32 v[6:7], vcc, v9, s88, v[4:5]
	v_lshl_add_u64 v[6:7], v[2:3], 1, v[6:7]
	v_cvt_pk_bf16_f32 v10, v134, v135
	v_cvt_pk_bf16_f32 v11, v136, v137
	v_cvt_pk_bf16_f32 v12, v130, v131
	v_cvt_pk_bf16_f32 v13, v132, v133
	global_store_dwordx4 v[6:7], v[10:13], off
	v_cvt_pk_bf16_f32 v14, v102, v103
	v_cvt_pk_bf16_f32 v15, v104, v105
	v_cvt_pk_bf16_f32 v16, v98, v99
	v_cvt_pk_bf16_f32 v17, v100, v101
	global_store_dwordx4 v[6:7], v[14:17], off offset:256
	v_add_u32_e32 v9, 128, v8
	v_mad_i64_i32 v[6:7], vcc, v9, s88, v[4:5]
	v_lshl_add_u64 v[6:7], v[2:3], 1, v[6:7]
	v_cvt_pk_bf16_f32 v10, v94, v95
	v_cvt_pk_bf16_f32 v11, v96, v97
	v_cvt_pk_bf16_f32 v12, v90, v91
	v_cvt_pk_bf16_f32 v13, v92, v93
	global_store_dwordx4 v[6:7], v[10:13], off
	v_cvt_pk_bf16_f32 v14, v62, v63
	v_cvt_pk_bf16_f32 v15, v64, v65
	v_cvt_pk_bf16_f32 v16, v58, v59
	v_cvt_pk_bf16_f32 v17, v60, v61
	global_store_dwordx4 v[6:7], v[14:17], off offset:256
	v_add_u32_e32 v9, 144, v8
	v_mad_i64_i32 v[6:7], vcc, v9, s88, v[4:5]
	v_lshl_add_u64 v[6:7], v[2:3], 1, v[6:7]
	v_cvt_pk_bf16_f32 v10, v86, v87
	v_cvt_pk_bf16_f32 v11, v88, v89
	v_cvt_pk_bf16_f32 v12, v82, v83
	v_cvt_pk_bf16_f32 v13, v84, v85
	global_store_dwordx4 v[6:7], v[10:13], off
	v_cvt_pk_bf16_f32 v14, v54, v55
	v_cvt_pk_bf16_f32 v15, v56, v57
	v_cvt_pk_bf16_f32 v16, v50, v51
	v_cvt_pk_bf16_f32 v17, v52, v53
	global_store_dwordx4 v[6:7], v[14:17], off offset:256
	v_add_u32_e32 v9, 160, v8
	v_mad_i64_i32 v[6:7], vcc, v9, s88, v[4:5]
	v_lshl_add_u64 v[6:7], v[2:3], 1, v[6:7]
	v_cvt_pk_bf16_f32 v10, v78, v79
	v_cvt_pk_bf16_f32 v11, v80, v81
	v_cvt_pk_bf16_f32 v12, v74, v75
	v_cvt_pk_bf16_f32 v13, v76, v77
	global_store_dwordx4 v[6:7], v[10:13], off
	v_cvt_pk_bf16_f32 v14, v46, v47
	v_cvt_pk_bf16_f32 v15, v48, v49
	v_cvt_pk_bf16_f32 v16, v42, v43
	v_cvt_pk_bf16_f32 v17, v44, v45
	global_store_dwordx4 v[6:7], v[14:17], off offset:256
	v_add_u32_e32 v9, 176, v8
	v_mad_i64_i32 v[6:7], vcc, v9, s88, v[4:5]
	v_lshl_add_u64 v[6:7], v[2:3], 1, v[6:7]
	v_cvt_pk_bf16_f32 v10, v70, v71
	v_cvt_pk_bf16_f32 v11, v72, v73
	v_cvt_pk_bf16_f32 v12, v66, v67
	v_cvt_pk_bf16_f32 v13, v68, v69
	global_store_dwordx4 v[6:7], v[10:13], off
	v_cvt_pk_bf16_f32 v14, v38, v39
	v_cvt_pk_bf16_f32 v15, v40, v41
	v_cvt_pk_bf16_f32 v16, v34, v35
	v_cvt_pk_bf16_f32 v17, v36, v37
	global_store_dwordx4 v[6:7], v[14:17], off offset:256
	s_andn2_b64 vcc, exec, s[42:43]
	s_mov_b64 s[0:1], -1
	s_cbranch_vccnz .LBB0_373
	s_branch .LBB0_456

.Lepi_old_ip8:
	s_nop 15
	s_nop 15
	v_mbcnt_lo_u32_b32 v2, -1, 0
	v_mbcnt_hi_u32_b32 v2, -1, v2
	s_add_i32 s0, s0, s81
	v_and_or_b32 v8, v2, 15, s0
	v_ashrrev_i32_e32 v2, 1, v2
	s_lshl_b32 s0, s4, 8
	v_and_b32_e32 v2, -8, v2
	s_or_b32 s0, s0, s6
	v_add_u32_e32 v2, s0, v2
	s_and_b32 s0, s4, -2
	v_mov_b64_e32 v[4:5], s[8:9]
	s_cmp_eq_u32 s0, 6
	v_mad_i64_i32 v[6:7], s[0:1], v8, s88, v[4:5]
	v_ashrrev_i32_e32 v3, 31, v2
	v_pk_mul_f32 v[4:5], v[160:161], s[14:15] op_sel_hi:[1,0]
	v_pk_mul_f32 v[10:11], v[158:159], s[14:15] op_sel_hi:[1,0]
	v_pk_mul_f32 v[18:19], v[156:157], s[14:15] op_sel_hi:[1,0]
	v_pk_mul_f32 v[20:21], v[154:155], s[14:15] op_sel_hi:[1,0]
	s_cselect_b64 s[0:1], -1, 0
	s_cmp_gt_i32 s4, 14
	v_cndmask_b32_e64 v14, v159, v11, s[0:1]
	v_cndmask_b32_e64 v16, v158, v10, s[0:1]
	v_cndmask_b32_e64 v12, v161, v5, s[0:1]
	v_cndmask_b32_e64 v15, v160, v4, s[0:1]
	v_cndmask_b32_e64 v10, v155, v21, s[0:1]
	v_cndmask_b32_e64 v13, v154, v20, s[0:1]
	v_cndmask_b32_e64 v9, v157, v19, s[0:1]
	v_cndmask_b32_e64 v11, v156, v18, s[0:1]
	s_cselect_b64 s[44:45], -1, 0
	s_cmp_lt_i32 s4, 15
	s_mov_b64 s[4:5], -1
	v_lshl_add_u64 v[4:5], v[6:7], 0, v[2:3]
	s_cbranch_scc1 .LBB0_393
	v_mul_f32_e32 v18, 0xbfb8aa3b, v13
	v_min_f32_e32 v18, 0x410c0000, v18
	v_exp_f32_e32 v20, v18
	v_mul_f32_e32 v18, 0xbfb8aa3b, v14
	v_min_f32_e32 v18, 0x410c0000, v18
	v_exp_f32_e32 v19, v18
	v_mul_f32_e32 v18, 0xbfb8aa3b, v10
	v_min_f32_e32 v18, 0x410c0000, v18
	v_exp_f32_e32 v21, v18
	v_mul_f32_e32 v18, 0xbfb8aa3b, v15
	v_min_f32_e32 v18, 0x410c0000, v18
	v_exp_f32_e32 v22, v18
	v_mul_f32_e32 v18, 0xbfb8aa3b, v11
	v_mul_f32_e32 v17, 0xbfb8aa3b, v16
	v_min_f32_e32 v18, 0x410c0000, v18
	v_min_f32_e32 v17, 0x410c0000, v17
	v_exp_f32_e32 v23, v18
	v_mul_f32_e32 v18, 0xbfb8aa3b, v12
	v_exp_f32_e32 v17, v17
	v_min_f32_e32 v18, 0x410c0000, v18
	v_exp_f32_e32 v24, v18
	v_mul_f32_e32 v18, 0xbfb8aa3b, v9
	v_min_f32_e32 v18, 0x410c0000, v18
	v_exp_f32_e32 v25, v18
	v_mov_b32_e32 v18, v1
	v_cvt_pk_fp8_f32 v18, v17, v19
	v_mov_b32_e32 v19, v1
	v_cvt_pk_fp8_f32 v19, v20, v21
	s_mov_b64 s[4:5], 0
	v_cvt_pk_fp8_f32 v18, v22, v24 op_sel:[0,0,1]
	v_cvt_pk_fp8_f32 v19, v23, v25 op_sel:[0,0,1]
	global_store_dwordx2 v[4:5], v[18:19], off offset:3840

.LBB0_476:
	v_readlane_b32 s6, v252, 15
	v_readlane_b32 s7, v252, 16
	v_cvt_f32_u32_e32 v0, v3
	v_sub_u32_e32 v5, 0, v3
	v_rcp_iflag_f32_e32 v0, v0
	s_nop 1
	global_atomic_add v4, v1, v236, s[6:7] sc0
	v_mul_f32_e32 v0, 0x4f7ffffe, v0
	v_cvt_u32_f32_e32 v0, v0
	v_mul_lo_u32 v5, v5, v0
	v_mul_hi_u32 v5, v0, v5
	v_add_u32_e32 v0, v0, v5
	s_waitcnt vmcnt(0)
	v_mul_hi_u32 v0, v4, v0
	v_mul_lo_u32 v5, v0, v3
	v_sub_u32_e32 v5, v4, v5
	v_add_u32_e32 v6, 1, v0
	v_cmp_ge_u32_e32 vcc, v5, v3
	v_add_u32_e32 v4, 1, v4
	s_nop 0
	v_cndmask_b32_e32 v0, v0, v6, vcc
	v_sub_u32_e32 v6, v5, v3
	v_cndmask_b32_e32 v5, v5, v6, vcc
	v_add_u32_e32 v6, 1, v0
	v_cmp_ge_u32_e32 vcc, v5, v3
	s_nop 1
	v_cndmask_b32_e32 v0, v0, v6, vcc
	v_mul_lo_u32 v5, v3, v0
	v_add_u32_e32 v3, v5, v3
	v_cmp_ne_u32_e32 vcc, v4, v3
	s_and_saveexec_b64 s[6:7], vcc
	s_xor_b64 s[6:7], exec, s[6:7]
	s_cbranch_execz .LBB0_490
	v_readlane_b32 s8, v252, 21
	v_readlane_b32 s9, v252, 22
	s_waitcnt lgkmcnt(0)
	s_nop 3
	global_load_dword v2, v1, s[8:9] sc1
	s_waitcnt vmcnt(0)
	v_cmp_eq_u32_e32 vcc, v2, v0
	s_and_saveexec_b64 s[8:9], vcc
	s_cbranch_execz .LBB0_489
	s_mov_b32 s13, 1
	s_mov_b64 s[10:11], 0
	s_branch .LBB0_480

.LBB0_505:
	s_or_b64 exec, exec, s[6:7]
	s_and_saveexec_b64 s[6:7], s[8:9]
	s_cbranch_execz .LBB0_507
	global_atomic_add v[2:3], v236, off
.LBB0_507:
	s_or_b64 exec, exec, s[6:7]
	s_waitcnt vmcnt(0)
	buffer_inv sc1
	s_waitcnt vmcnt(0)
.LBB0_508:
	s_or_b64 exec, exec, s[4:5]
	s_waitcnt lgkmcnt(0)
	s_barrier

.LBB0_1037:
	v_readlane_b32 s4, v252, 15
	v_readlane_b32 s5, v252, 16
	v_cvt_f32_u32_e32 v0, v3
	v_sub_u32_e32 v5, 0, v3
	v_rcp_iflag_f32_e32 v0, v0
	s_nop 1
	global_atomic_add v4, v1, v236, s[4:5] sc0
	v_mul_f32_e32 v0, 0x4f7ffffe, v0
	v_cvt_u32_f32_e32 v0, v0
	v_mul_lo_u32 v5, v5, v0
	v_mul_hi_u32 v5, v0, v5
	v_add_u32_e32 v0, v0, v5
	s_waitcnt vmcnt(0)
	v_mul_hi_u32 v0, v4, v0
	v_mul_lo_u32 v5, v0, v3
	v_sub_u32_e32 v5, v4, v5
	v_add_u32_e32 v6, 1, v0
	v_cmp_ge_u32_e32 vcc, v5, v3
	v_add_u32_e32 v4, 1, v4
	s_nop 0
	v_cndmask_b32_e32 v0, v0, v6, vcc
	v_sub_u32_e32 v6, v5, v3
	v_cndmask_b32_e32 v5, v5, v6, vcc
	v_add_u32_e32 v6, 1, v0
	v_cmp_ge_u32_e32 vcc, v5, v3
	s_nop 1
	v_cndmask_b32_e32 v0, v0, v6, vcc
	v_mul_lo_u32 v5, v3, v0
	v_add_u32_e32 v3, v5, v3
	v_cmp_ne_u32_e32 vcc, v4, v3
	s_and_saveexec_b64 s[4:5], vcc
	s_xor_b64 s[4:5], exec, s[4:5]
	s_cbranch_execz .LBB0_1051
	v_readlane_b32 s6, v252, 21
	v_readlane_b32 s7, v252, 22
	s_waitcnt lgkmcnt(0)
	s_nop 3
	global_load_dword v2, v1, s[6:7] sc1
	s_waitcnt vmcnt(0)
	v_cmp_eq_u32_e32 vcc, v2, v0
	s_and_saveexec_b64 s[6:7], vcc
	s_cbranch_execz .LBB0_1050
	s_mov_b32 s13, 1
	s_mov_b64 s[8:9], 0
	s_branch .LBB0_1041

.LBB0_1498:
	v_readlane_b32 s0, v252, 15
	v_readlane_b32 s1, v252, 16
	v_cvt_f32_u32_e32 v0, v3
	v_sub_u32_e32 v5, 0, v3
	v_rcp_iflag_f32_e32 v0, v0
	s_nop 1
	global_atomic_add v4, v1, v236, s[0:1] sc0
	v_mul_f32_e32 v0, 0x4f7ffffe, v0
	v_cvt_u32_f32_e32 v0, v0
	v_mul_lo_u32 v5, v5, v0
	v_mul_hi_u32 v5, v0, v5
	v_add_u32_e32 v0, v0, v5
	s_waitcnt vmcnt(0)
	v_mul_hi_u32 v0, v4, v0
	v_mul_lo_u32 v5, v0, v3
	v_sub_u32_e32 v5, v4, v5
	v_add_u32_e32 v6, 1, v0
	v_cmp_ge_u32_e32 vcc, v5, v3
	v_add_u32_e32 v4, 1, v4
	s_nop 0
	v_cndmask_b32_e32 v0, v0, v6, vcc
	v_sub_u32_e32 v6, v5, v3
	v_cndmask_b32_e32 v5, v5, v6, vcc
	v_add_u32_e32 v6, 1, v0
	v_cmp_ge_u32_e32 vcc, v5, v3
	s_nop 1
	v_cndmask_b32_e32 v0, v0, v6, vcc
	v_mul_lo_u32 v5, v3, v0
	v_add_u32_e32 v3, v5, v3
	v_cmp_ne_u32_e32 vcc, v4, v3
	s_and_saveexec_b64 s[0:1], vcc
	s_xor_b64 s[6:7], exec, s[0:1]
	s_cbranch_execz .LBB0_1512
	v_readlane_b32 s0, v252, 21
	v_readlane_b32 s1, v252, 22
	s_waitcnt lgkmcnt(0)
	s_nop 3
	global_load_dword v2, v1, s[0:1] sc1
	s_waitcnt vmcnt(0)
	v_cmp_eq_u32_e32 vcc, v2, v0
	s_and_saveexec_b64 s[8:9], vcc
	s_cbranch_execz .LBB0_1511
	s_mov_b32 s0, 1
	s_mov_b64 s[10:11], 0
	s_branch .LBB0_1502

.LBB0_1527:
	s_or_b64 exec, exec, s[6:7]
	s_and_saveexec_b64 s[6:7], s[8:9]
	s_cbranch_execz .LBB0_1529
	global_atomic_add v[2:3], v236, off
.LBB0_1529:
	s_or_b64 exec, exec, s[6:7]
	s_waitcnt vmcnt(0)
	buffer_inv sc1
	s_waitcnt vmcnt(0)
.LBB0_1530:
	s_or_b64 exec, exec, s[4:5]
	s_waitcnt lgkmcnt(0)
	s_barrier

.LBB0_1590:
	v_readlane_b32 s4, v252, 15
	v_readlane_b32 s5, v252, 16
	v_cvt_f32_u32_e32 v0, v3
	v_sub_u32_e32 v5, 0, v3
	v_rcp_iflag_f32_e32 v0, v0
	s_nop 1
	global_atomic_add v4, v1, v236, s[4:5] sc0
	v_mul_f32_e32 v0, 0x4f7ffffe, v0
	v_cvt_u32_f32_e32 v0, v0
	v_mul_lo_u32 v5, v5, v0
	v_mul_hi_u32 v5, v0, v5
	v_add_u32_e32 v0, v0, v5
	s_waitcnt vmcnt(0)
	v_mul_hi_u32 v0, v4, v0
	v_mul_lo_u32 v5, v0, v3
	v_sub_u32_e32 v5, v4, v5
	v_add_u32_e32 v6, 1, v0
	v_cmp_ge_u32_e32 vcc, v5, v3
	v_add_u32_e32 v4, 1, v4
	s_nop 0
	v_cndmask_b32_e32 v0, v0, v6, vcc
	v_sub_u32_e32 v6, v5, v3
	v_cndmask_b32_e32 v5, v5, v6, vcc
	v_add_u32_e32 v6, 1, v0
	v_cmp_ge_u32_e32 vcc, v5, v3
	s_nop 1
	v_cndmask_b32_e32 v0, v0, v6, vcc
	v_mul_lo_u32 v5, v3, v0
	v_add_u32_e32 v3, v5, v3
	v_cmp_ne_u32_e32 vcc, v4, v3
	s_and_saveexec_b64 s[4:5], vcc
	s_xor_b64 s[4:5], exec, s[4:5]
	s_cbranch_execz .LBB0_1604
	v_readlane_b32 s6, v252, 21
	v_readlane_b32 s7, v252, 22
	s_waitcnt lgkmcnt(0)
	s_nop 3
	global_load_dword v2, v1, s[6:7] sc1
	s_waitcnt vmcnt(0)
	v_cmp_eq_u32_e32 vcc, v2, v0
	s_and_saveexec_b64 s[6:7], vcc
	s_cbranch_execz .LBB0_1603
	s_mov_b32 s26, 1
	s_mov_b64 s[8:9], 0
	s_branch .LBB0_1594

.LBB0_1694:
	v_readlane_b32 s6, v252, 15
	v_readlane_b32 s7, v252, 16
	v_cvt_f32_u32_e32 v0, v3
	v_sub_u32_e32 v5, 0, v3
	v_rcp_iflag_f32_e32 v0, v0
	s_nop 1
	global_atomic_add v4, v1, v236, s[6:7] sc0
	v_mul_f32_e32 v0, 0x4f7ffffe, v0
	v_cvt_u32_f32_e32 v0, v0
	v_mul_lo_u32 v5, v5, v0
	v_mul_hi_u32 v5, v0, v5
	v_add_u32_e32 v0, v0, v5
	s_waitcnt vmcnt(0)
	v_mul_hi_u32 v0, v4, v0
	v_mul_lo_u32 v5, v0, v3
	v_sub_u32_e32 v5, v4, v5
	v_add_u32_e32 v6, 1, v0
	v_cmp_ge_u32_e32 vcc, v5, v3
	v_add_u32_e32 v4, 1, v4
	s_nop 0
	v_cndmask_b32_e32 v0, v0, v6, vcc
	v_sub_u32_e32 v6, v5, v3
	v_cndmask_b32_e32 v5, v5, v6, vcc
	v_add_u32_e32 v6, 1, v0
	v_cmp_ge_u32_e32 vcc, v5, v3
	s_nop 1
	v_cndmask_b32_e32 v0, v0, v6, vcc
	v_mul_lo_u32 v5, v3, v0
	v_add_u32_e32 v3, v5, v3
	v_cmp_ne_u32_e32 vcc, v4, v3
	s_and_saveexec_b64 s[6:7], vcc
	s_xor_b64 s[6:7], exec, s[6:7]
	s_cbranch_execz .LBB0_1708
	v_readlane_b32 s8, v252, 21
	v_readlane_b32 s9, v252, 22
	s_waitcnt lgkmcnt(0)
	s_nop 3
	global_load_dword v2, v1, s[8:9] sc1
	s_waitcnt vmcnt(0)
	v_cmp_eq_u32_e32 vcc, v2, v0
	s_and_saveexec_b64 s[8:9], vcc
	s_cbranch_execz .LBB0_1707
	s_mov_b32 s26, 1
	s_mov_b64 s[10:11], 0
	s_branch .LBB0_1698

.LBB0_1723:
	s_or_b64 exec, exec, s[6:7]
	s_and_saveexec_b64 s[6:7], s[8:9]
	s_cbranch_execz .LBB0_1725
	global_atomic_add v[2:3], v236, off
.LBB0_1725:
	s_or_b64 exec, exec, s[6:7]
	s_waitcnt vmcnt(0)
	buffer_inv sc1
	s_waitcnt vmcnt(0)
.LBB0_1726:
	s_or_b64 exec, exec, s[4:5]
	s_waitcnt lgkmcnt(0)
	s_barrier

.LBB0_1955:
	s_or_b64 exec, exec, s[6:7]
	s_and_saveexec_b64 s[6:7], s[8:9]
	s_cbranch_execz .LBB0_1957
	global_atomic_add v[2:3], v236, off
.LBB0_1957:
	s_or_b64 exec, exec, s[6:7]
	s_waitcnt vmcnt(0)
	buffer_inv sc1
	s_waitcnt vmcnt(0)
.LBB0_1958:
	s_or_b64 exec, exec, s[4:5]
	s_waitcnt lgkmcnt(0)
	s_barrier

.LBB0_2007:
	s_lshl_b32 s4, s23, 10
	v_mbcnt_lo_u32_b32 v0, -1, 0
	v_mbcnt_hi_u32_b32 v0, -1, v0
	s_and_b32 s4, s4, 0x400
	v_readlane_b32 s5, v254, 53
	v_lshlrev_b32_e32 v2, 1, v0
	s_add_i32 s4, s5, s4
	v_and_b32_e32 v2, 0xffffffe0, v2
	v_add_u32_e32 v10, s4, v2
	ds_read_b128 v[2:5], v10
	ds_read_b128 v[6:9], v10 offset:16
	s_mov_b32 s26, 0xc01d265f
	s_lshl_b32 s4, s48, 8
	v_readlane_b32 s5, v254, 47
	s_waitcnt lgkmcnt(0)
	v_pk_mul_f32 v[18:19], v[4:5], s[26:27] op_sel_hi:[1,0]
	v_pk_mul_f32 v[20:21], v[2:3], s[26:27] op_sel_hi:[1,0]
	ds_read_b128 v[2:5], v10 offset:512
	s_add_i32 s4, s4, s5
	v_pk_add_f32 v[28:29], v[146:147], v[6:7]
	s_mov_b32 s23, 0xc0e00000
	v_med3_f32 v28, v28, s23, v243
	s_waitcnt lgkmcnt(0)
	v_pk_mul_f32 v[14:15], v[4:5], s[26:27] op_sel_hi:[1,0]
	v_pk_mul_f32 v[16:17], v[2:3], s[26:27] op_sel_hi:[1,0]
	ds_read_b128 v[2:5], v10 offset:528
	v_and_or_b32 v10, v0, 15, s4
	v_and_b32_e32 v0, -16, v0
	v_add_u32_e32 v22, v10, v0
	v_pk_fma_f32 v[10:11], v[150:151], s[26:27], v[20:21] op_sel_hi:[1,0,1]
	v_med3_f32 v29, v29, s23, v243
	v_max_f32_e32 v10, 0xc1898193, v10
	v_max_f32_e32 v11, 0xc1898193, v11
	v_exp_f32_e32 v12, v10
	v_exp_f32_e32 v13, v11
	s_mov_b32 s48, 0xbfd083aa
	v_pk_fma_f32 v[28:29], v[28:29], s[48:49], s[48:49] op_sel_hi:[1,0,0]
	v_pk_add_f32 v[26:27], v[148:149], v[8:9]
	v_pk_add_f32 v[12:13], v[12:13], 1.0 op_sel_hi:[1,0]
	v_med3_f32 v26, v26, s23, v243
	v_rcp_f32_e32 v12, v12
	v_rcp_f32_e32 v13, v13
	v_med3_f32 v27, v27, s23, v243
	v_pk_fma_f32 v[26:27], v[26:27], s[48:49], s[48:49] op_sel_hi:[1,0,0]
	v_pk_add_f32 v[30:31], v[138:139], v[6:7]
	v_pk_mul_f32 v[10:11], v[10:11], v[12:13]
	v_med3_f32 v30, v30, s23, v243
	v_pk_mul_f32 v[12:13], v[28:29], v[10:11]
	v_pk_fma_f32 v[10:11], v[152:153], s[26:27], v[18:19] op_sel_hi:[1,0,1]
	v_med3_f32 v31, v31, s23, v243
	v_max_f32_e32 v10, 0xc1898193, v10
	v_max_f32_e32 v11, 0xc1898193, v11
	v_exp_f32_e32 v28, v10
	v_exp_f32_e32 v29, v11
	v_pk_fma_f32 v[30:31], v[30:31], s[48:49], s[48:49] op_sel_hi:[1,0,0]
	v_pk_add_f32 v[32:33], v[122:123], v[6:7]
	s_lshl_b32 s4, s50, 7
	v_pk_add_f32 v[28:29], v[28:29], 1.0 op_sel_hi:[1,0]
	v_med3_f32 v32, v32, s23, v243
	v_rcp_f32_e32 v28, v28
	v_rcp_f32_e32 v29, v29
	v_med3_f32 v33, v33, s23, v243
	v_pk_fma_f32 v[32:33], v[32:33], s[48:49], s[48:49] op_sel_hi:[1,0,0]
	v_readlane_b32 s5, v254, 49
	v_pk_mul_f32 v[10:11], v[10:11], v[28:29]
	v_pk_add_f32 v[28:29], v[140:141], v[8:9]
	v_pk_mul_f32 v[26:27], v[26:27], v[10:11]
	v_mov_b32_e32 v10, v1
	v_cvt_pk_fp8_f32 v10, v12, v13
	v_pk_fma_f32 v[12:13], v[142:143], s[26:27], v[20:21] op_sel_hi:[1,0,1]
	v_mov_b32_e32 v11, v1
	v_max_f32_e32 v12, 0xc1898193, v12
	v_max_f32_e32 v13, 0xc1898193, v13
	v_cvt_pk_fp8_f32 v10, v26, v27 op_sel:[0,0,1]
	v_exp_f32_e32 v26, v12
	v_exp_f32_e32 v27, v13
	v_med3_f32 v28, v28, s23, v243
	v_med3_f32 v29, v29, s23, v243
	v_pk_fma_f32 v[28:29], v[28:29], s[48:49], s[48:49] op_sel_hi:[1,0,0]
	v_pk_add_f32 v[26:27], v[26:27], 1.0 op_sel_hi:[1,0]
	v_ashrrev_i32_e32 v23, 31, v22
	v_rcp_f32_e32 v26, v26
	v_rcp_f32_e32 v27, v27
	s_or_b32 s4, s4, s5
	v_lshlrev_b64 v[24:25], 10, v[22:23]
	s_ashr_i32 s5, s4, 31
	v_pk_mul_f32 v[12:13], v[12:13], v[26:27]
	v_pk_fma_f32 v[26:27], v[144:145], s[26:27], v[18:19] op_sel_hi:[1,0,1]
	v_pk_mul_f32 v[12:13], v[30:31], v[12:13]
	v_max_f32_e32 v26, 0xc1898193, v26
	v_max_f32_e32 v27, 0xc1898193, v27
	v_exp_f32_e32 v30, v26
	v_exp_f32_e32 v31, v27
	v_cvt_pk_fp8_f32 v11, v12, v13
	v_pk_fma_f32 v[12:13], v[134:135], s[26:27], v[20:21] op_sel_hi:[1,0,1]
	v_lshl_add_u64 v[24:25], s[12:13], 0, v[24:25]
	v_pk_add_f32 v[30:31], v[30:31], 1.0 op_sel_hi:[1,0]
	v_max_f32_e32 v12, 0xc1898193, v12
	v_rcp_f32_e32 v30, v30
	v_rcp_f32_e32 v31, v31
	v_max_f32_e32 v13, 0xc1898193, v13
	v_lshl_add_u64 v[24:25], v[24:25], 0, s[4:5]
	s_and_b64 vcc, exec, s[0:1]
	v_pk_mul_f32 v[26:27], v[26:27], v[30:31]
	v_pk_add_f32 v[30:31], v[130:131], v[6:7]
	v_pk_mul_f32 v[26:27], v[28:29], v[26:27]
	v_med3_f32 v30, v30, s23, v243
	v_cvt_pk_fp8_f32 v11, v26, v27 op_sel:[0,0,1]
	v_exp_f32_e32 v26, v12
	v_exp_f32_e32 v27, v13
	v_med3_f32 v31, v31, s23, v243
	v_pk_fma_f32 v[30:31], v[30:31], s[48:49], s[48:49] op_sel_hi:[1,0,0]
	v_pk_add_f32 v[28:29], v[132:133], v[8:9]
	v_pk_add_f32 v[26:27], v[26:27], 1.0 op_sel_hi:[1,0]
	v_med3_f32 v28, v28, s23, v243
	v_rcp_f32_e32 v26, v26
	v_rcp_f32_e32 v27, v27
	v_med3_f32 v29, v29, s23, v243
	v_pk_fma_f32 v[28:29], v[28:29], s[48:49], s[48:49] op_sel_hi:[1,0,0]
	v_pk_mul_f32 v[12:13], v[12:13], v[26:27]
	s_nop 0
	v_pk_mul_f32 v[26:27], v[30:31], v[12:13]
	v_pk_fma_f32 v[12:13], v[136:137], s[26:27], v[18:19] op_sel_hi:[1,0,1]
	s_nop 0
	v_max_f32_e32 v12, 0xc1898193, v12
	v_max_f32_e32 v13, 0xc1898193, v13
	v_exp_f32_e32 v30, v12
	v_exp_f32_e32 v31, v13
	s_nop 0
	v_pk_add_f32 v[30:31], v[30:31], 1.0 op_sel_hi:[1,0]
	s_nop 0
	v_rcp_f32_e32 v30, v30
	v_rcp_f32_e32 v31, v31
	s_nop 0
	v_pk_mul_f32 v[12:13], v[12:13], v[30:31]
	s_nop 0
	v_pk_mul_f32 v[28:29], v[28:29], v[12:13]
	v_mov_b32_e32 v12, v1
	v_cvt_pk_fp8_f32 v12, v26, v27
	v_pk_fma_f32 v[26:27], v[126:127], s[26:27], v[20:21] op_sel_hi:[1,0,1]
	v_mov_b32_e32 v13, v1
	v_max_f32_e32 v26, 0xc1898193, v26
	v_max_f32_e32 v27, 0xc1898193, v27
	v_cvt_pk_fp8_f32 v12, v28, v29 op_sel:[0,0,1]
	v_exp_f32_e32 v28, v26
	v_exp_f32_e32 v29, v27
	v_pk_add_f32 v[30:31], v[124:125], v[8:9]
	v_permlane32_swap_b32_e32 v10, v12
	v_pk_add_f32 v[28:29], v[28:29], 1.0 op_sel_hi:[1,0]
	v_med3_f32 v30, v30, s23, v243
	v_rcp_f32_e32 v28, v28
	v_rcp_f32_e32 v29, v29
	v_med3_f32 v31, v31, s23, v243
	v_pk_fma_f32 v[30:31], v[30:31], s[48:49], s[48:49] op_sel_hi:[1,0,0]
	v_pk_mul_f32 v[26:27], v[26:27], v[28:29]
	v_pk_fma_f32 v[28:29], v[128:129], s[26:27], v[18:19] op_sel_hi:[1,0,1]
	v_pk_mul_f32 v[26:27], v[32:33], v[26:27]
	v_max_f32_e32 v28, 0xc1898193, v28
	v_max_f32_e32 v29, 0xc1898193, v29
	v_exp_f32_e32 v32, v28
	v_exp_f32_e32 v33, v29
	v_cvt_pk_fp8_f32 v13, v26, v27
	s_waitcnt lgkmcnt(0)
	v_pk_add_f32 v[26:27], v[116:117], v[4:5]
	v_pk_add_f32 v[32:33], v[32:33], 1.0 op_sel_hi:[1,0]
	s_nop 0
	v_rcp_f32_e32 v32, v32
	v_rcp_f32_e32 v33, v33
	v_med3_f32 v26, v26, s23, v243
	v_med3_f32 v27, v27, s23, v243
	v_pk_fma_f32 v[26:27], v[26:27], s[48:49], s[48:49] op_sel_hi:[1,0,0]
	v_pk_mul_f32 v[28:29], v[28:29], v[32:33]
	v_pk_add_f32 v[32:33], v[90:91], v[2:3]
	v_pk_mul_f32 v[28:29], v[30:31], v[28:29]
	v_pk_add_f32 v[30:31], v[106:107], v[2:3]
	v_cvt_pk_fp8_f32 v13, v28, v29 op_sel:[0,0,1]
	v_pk_add_f32 v[28:29], v[114:115], v[2:3]
	v_med3_f32 v30, v30, s23, v243
	v_med3_f32 v28, v28, s23, v243
	v_permlane32_swap_b32_e32 v11, v13
	s_nop 1
	v_permlane16_swap_b32_e32 v10, v11
	v_permlane16_swap_b32_e32 v12, v13
	global_store_dwordx4 v[24:25], v[10:13], off
	v_med3_f32 v29, v29, s23, v243
	v_pk_fma_f32 v[28:29], v[28:29], s[48:49], s[48:49] op_sel_hi:[1,0,0]
	v_pk_fma_f32 v[10:11], v[118:119], s[26:27], v[16:17] op_sel_hi:[1,0,1]
	v_med3_f32 v31, v31, s23, v243
	v_max_f32_e32 v10, 0xc1898193, v10
	v_max_f32_e32 v11, 0xc1898193, v11
	v_exp_f32_e32 v12, v10
	v_exp_f32_e32 v13, v11
	v_pk_fma_f32 v[30:31], v[30:31], s[48:49], s[48:49] op_sel_hi:[1,0,0]
	v_med3_f32 v32, v32, s23, v243
	v_med3_f32 v33, v33, s23, v243
	v_pk_add_f32 v[12:13], v[12:13], 1.0 op_sel_hi:[1,0]
	v_pk_fma_f32 v[32:33], v[32:33], s[48:49], s[48:49] op_sel_hi:[1,0,0]
	v_rcp_f32_e32 v12, v12
	v_rcp_f32_e32 v13, v13
	s_nop 0
	v_pk_mul_f32 v[10:11], v[10:11], v[12:13]
	s_nop 0
	v_pk_mul_f32 v[12:13], v[28:29], v[10:11]
	v_pk_fma_f32 v[10:11], v[120:121], s[26:27], v[14:15] op_sel_hi:[1,0,1]
	s_nop 0
	v_max_f32_e32 v10, 0xc1898193, v10
	v_max_f32_e32 v11, 0xc1898193, v11
	v_exp_f32_e32 v28, v10
	v_exp_f32_e32 v29, v11
	s_nop 0
	v_pk_add_f32 v[28:29], v[28:29], 1.0 op_sel_hi:[1,0]
	s_nop 0
	v_rcp_f32_e32 v28, v28
	v_rcp_f32_e32 v29, v29
	s_nop 0
	v_pk_mul_f32 v[10:11], v[10:11], v[28:29]
	s_nop 0
	v_pk_mul_f32 v[26:27], v[26:27], v[10:11]
	v_mov_b32_e32 v10, v1
	v_cvt_pk_fp8_f32 v10, v12, v13
	v_pk_fma_f32 v[12:13], v[110:111], s[26:27], v[16:17] op_sel_hi:[1,0,1]
	v_mov_b32_e32 v11, v1
	v_max_f32_e32 v12, 0xc1898193, v12
	v_max_f32_e32 v13, 0xc1898193, v13
	v_cvt_pk_fp8_f32 v10, v26, v27 op_sel:[0,0,1]
	v_exp_f32_e32 v26, v12
	v_exp_f32_e32 v27, v13
	v_pk_add_f32 v[28:29], v[108:109], v[4:5]
	v_pk_add_f32 v[26:27], v[26:27], 1.0 op_sel_hi:[1,0]
	s_nop 0
	v_rcp_f32_e32 v26, v26
	v_rcp_f32_e32 v27, v27
	v_med3_f32 v28, v28, s23, v243
	v_med3_f32 v29, v29, s23, v243
	v_pk_fma_f32 v[28:29], v[28:29], s[48:49], s[48:49] op_sel_hi:[1,0,0]
	v_pk_mul_f32 v[12:13], v[12:13], v[26:27]
	v_pk_fma_f32 v[26:27], v[112:113], s[26:27], v[14:15] op_sel_hi:[1,0,1]
	v_pk_mul_f32 v[12:13], v[30:31], v[12:13]
	v_max_f32_e32 v26, 0xc1898193, v26
	v_max_f32_e32 v27, 0xc1898193, v27
	v_exp_f32_e32 v30, v26
	v_exp_f32_e32 v31, v27
	v_cvt_pk_fp8_f32 v11, v12, v13
	v_pk_fma_f32 v[12:13], v[102:103], s[26:27], v[16:17] op_sel_hi:[1,0,1]
	v_pk_add_f32 v[30:31], v[30:31], 1.0 op_sel_hi:[1,0]
	s_nop 0
	v_rcp_f32_e32 v30, v30
	v_rcp_f32_e32 v31, v31
	v_max_f32_e32 v12, 0xc1898193, v12
	v_max_f32_e32 v13, 0xc1898193, v13
	v_pk_mul_f32 v[26:27], v[26:27], v[30:31]
	s_nop 0
	v_pk_mul_f32 v[26:27], v[28:29], v[26:27]
	v_pk_add_f32 v[30:31], v[98:99], v[2:3]
	v_cvt_pk_fp8_f32 v11, v26, v27 op_sel:[0,0,1]
	v_exp_f32_e32 v26, v12
	v_exp_f32_e32 v27, v13
	v_med3_f32 v30, v30, s23, v243
	v_med3_f32 v31, v31, s23, v243
	v_pk_fma_f32 v[30:31], v[30:31], s[48:49], s[48:49] op_sel_hi:[1,0,0]
	v_pk_add_f32 v[26:27], v[26:27], 1.0 op_sel_hi:[1,0]
	v_pk_add_f32 v[28:29], v[100:101], v[4:5]
	v_rcp_f32_e32 v26, v26
	v_rcp_f32_e32 v27, v27
	v_med3_f32 v28, v28, s23, v243
	v_med3_f32 v29, v29, s23, v243
	v_pk_fma_f32 v[28:29], v[28:29], s[48:49], s[48:49] op_sel_hi:[1,0,0]
	v_pk_mul_f32 v[12:13], v[12:13], v[26:27]
	s_nop 0
	v_pk_mul_f32 v[26:27], v[30:31], v[12:13]
	v_pk_fma_f32 v[12:13], v[104:105], s[26:27], v[14:15] op_sel_hi:[1,0,1]
	s_nop 0
	v_max_f32_e32 v12, 0xc1898193, v12
	v_max_f32_e32 v13, 0xc1898193, v13
	v_exp_f32_e32 v30, v12
	v_exp_f32_e32 v31, v13
	s_nop 0
	v_pk_add_f32 v[30:31], v[30:31], 1.0 op_sel_hi:[1,0]
	s_nop 0
	v_rcp_f32_e32 v30, v30
	v_rcp_f32_e32 v31, v31
	s_nop 0
	v_pk_mul_f32 v[12:13], v[12:13], v[30:31]
	s_nop 0
	v_pk_mul_f32 v[28:29], v[28:29], v[12:13]
	v_mov_b32_e32 v12, v1
	v_cvt_pk_fp8_f32 v12, v26, v27
	v_pk_fma_f32 v[26:27], v[94:95], s[26:27], v[16:17] op_sel_hi:[1,0,1]
	v_mov_b32_e32 v13, v1
	v_max_f32_e32 v26, 0xc1898193, v26
	v_max_f32_e32 v27, 0xc1898193, v27
	v_cvt_pk_fp8_f32 v12, v28, v29 op_sel:[0,0,1]
	v_exp_f32_e32 v28, v26
	v_exp_f32_e32 v29, v27
	v_pk_add_f32 v[30:31], v[92:93], v[4:5]
	v_permlane32_swap_b32_e32 v10, v12
	v_pk_add_f32 v[28:29], v[28:29], 1.0 op_sel_hi:[1,0]
	v_med3_f32 v30, v30, s23, v243
	v_rcp_f32_e32 v28, v28
	v_rcp_f32_e32 v29, v29
	v_med3_f32 v31, v31, s23, v243
	v_pk_fma_f32 v[30:31], v[30:31], s[48:49], s[48:49] op_sel_hi:[1,0,0]
	v_pk_mul_f32 v[26:27], v[26:27], v[28:29]
	v_pk_fma_f32 v[28:29], v[96:97], s[26:27], v[14:15] op_sel_hi:[1,0,1]
	v_pk_mul_f32 v[26:27], v[32:33], v[26:27]
	v_max_f32_e32 v28, 0xc1898193, v28
	v_max_f32_e32 v29, 0xc1898193, v29
	v_exp_f32_e32 v32, v28
	v_exp_f32_e32 v33, v29
	v_cvt_pk_fp8_f32 v13, v26, v27
	v_pk_add_f32 v[26:27], v[82:83], v[6:7]
	v_pk_add_f32 v[32:33], v[32:33], 1.0 op_sel_hi:[1,0]
	s_nop 0
	v_rcp_f32_e32 v32, v32
	v_rcp_f32_e32 v33, v33
	v_med3_f32 v26, v26, s23, v243
	v_med3_f32 v27, v27, s23, v243
	v_pk_fma_f32 v[26:27], v[26:27], s[48:49], s[48:49] op_sel_hi:[1,0,0]
	v_pk_mul_f32 v[28:29], v[28:29], v[32:33]
	s_nop 0
	v_pk_mul_f32 v[28:29], v[30:31], v[28:29]
	s_nop 0
	v_cvt_pk_fp8_f32 v13, v28, v29 op_sel:[0,0,1]
	v_pk_add_f32 v[28:29], v[74:75], v[6:7]
	s_nop 0
	v_permlane32_swap_b32_e32 v11, v13
	s_nop 1
	v_permlane16_swap_b32_e32 v10, v11
	v_permlane16_swap_b32_e32 v12, v13
	global_store_dwordx4 v[24:25], v[10:13], off offset:64
	v_pk_add_f32 v[24:25], v[84:85], v[8:9]
	v_med3_f32 v28, v28, s23, v243
	v_add_u32_e32 v10, 0x80, v22
	v_ashrrev_i32_e32 v11, 31, v10
	v_lshlrev_b64 v[22:23], 10, v[10:11]
	v_pk_fma_f32 v[10:11], v[86:87], s[26:27], v[20:21] op_sel_hi:[1,0,1]
	v_med3_f32 v24, v24, s23, v243
	v_max_f32_e32 v10, 0xc1898193, v10
	v_max_f32_e32 v11, 0xc1898193, v11
	v_exp_f32_e32 v12, v10
	v_exp_f32_e32 v13, v11
	v_med3_f32 v25, v25, s23, v243
	v_pk_fma_f32 v[24:25], v[24:25], s[48:49], s[48:49] op_sel_hi:[1,0,0]
	v_med3_f32 v29, v29, s23, v243
	v_pk_add_f32 v[12:13], v[12:13], 1.0 op_sel_hi:[1,0]
	v_pk_fma_f32 v[28:29], v[28:29], s[48:49], s[48:49] op_sel_hi:[1,0,0]
	v_rcp_f32_e32 v12, v12
	v_rcp_f32_e32 v13, v13
	s_nop 0
	v_pk_mul_f32 v[10:11], v[10:11], v[12:13]
	s_nop 0
	v_pk_mul_f32 v[12:13], v[26:27], v[10:11]
	v_pk_fma_f32 v[10:11], v[88:89], s[26:27], v[18:19] op_sel_hi:[1,0,1]
	s_nop 0
	v_max_f32_e32 v10, 0xc1898193, v10
	v_max_f32_e32 v11, 0xc1898193, v11
	v_exp_f32_e32 v26, v10
	v_exp_f32_e32 v27, v11
	s_nop 0
	v_pk_add_f32 v[26:27], v[26:27], 1.0 op_sel_hi:[1,0]
	s_nop 0
	v_rcp_f32_e32 v26, v26
	v_rcp_f32_e32 v27, v27
	s_nop 0
	v_pk_mul_f32 v[10:11], v[10:11], v[26:27]
	s_nop 0
	v_pk_mul_f32 v[24:25], v[24:25], v[10:11]
	v_mov_b32_e32 v10, v1
	v_cvt_pk_fp8_f32 v10, v12, v13
	v_pk_fma_f32 v[12:13], v[78:79], s[26:27], v[20:21] op_sel_hi:[1,0,1]
	v_mov_b32_e32 v11, v1
	v_max_f32_e32 v12, 0xc1898193, v12
	v_max_f32_e32 v13, 0xc1898193, v13
	v_cvt_pk_fp8_f32 v10, v24, v25 op_sel:[0,0,1]
	v_exp_f32_e32 v24, v12
	v_exp_f32_e32 v25, v13
	v_pk_add_f32 v[26:27], v[76:77], v[8:9]
	v_pk_add_f32 v[24:25], v[24:25], 1.0 op_sel_hi:[1,0]
	s_nop 0
	v_rcp_f32_e32 v24, v24
	v_rcp_f32_e32 v25, v25
	v_med3_f32 v26, v26, s23, v243
	v_med3_f32 v27, v27, s23, v243
	v_pk_fma_f32 v[26:27], v[26:27], s[48:49], s[48:49] op_sel_hi:[1,0,0]
	v_pk_mul_f32 v[12:13], v[12:13], v[24:25]
	v_pk_fma_f32 v[24:25], v[80:81], s[26:27], v[18:19] op_sel_hi:[1,0,1]
	v_pk_mul_f32 v[12:13], v[28:29], v[12:13]
	v_max_f32_e32 v24, 0xc1898193, v24
	v_max_f32_e32 v25, 0xc1898193, v25
	v_exp_f32_e32 v28, v24
	v_exp_f32_e32 v29, v25
	v_cvt_pk_fp8_f32 v11, v12, v13
	v_pk_fma_f32 v[12:13], v[70:71], s[26:27], v[20:21] op_sel_hi:[1,0,1]
	v_pk_fma_f32 v[20:21], v[62:63], s[26:27], v[20:21] op_sel_hi:[1,0,1]
	v_pk_add_f32 v[28:29], v[28:29], 1.0 op_sel_hi:[1,0]
	v_max_f32_e32 v12, 0xc1898193, v12
	v_rcp_f32_e32 v28, v28
	v_rcp_f32_e32 v29, v29
	v_max_f32_e32 v13, 0xc1898193, v13
	v_max_f32_e32 v20, 0xc1898193, v20
	v_max_f32_e32 v21, 0xc1898193, v21
	v_pk_mul_f32 v[24:25], v[24:25], v[28:29]
	v_pk_add_f32 v[28:29], v[66:67], v[6:7]
	v_pk_mul_f32 v[24:25], v[26:27], v[24:25]
	v_med3_f32 v28, v28, s23, v243
	v_cvt_pk_fp8_f32 v11, v24, v25 op_sel:[0,0,1]
	v_exp_f32_e32 v24, v12
	v_exp_f32_e32 v25, v13
	v_med3_f32 v29, v29, s23, v243
	v_pk_fma_f32 v[28:29], v[28:29], s[48:49], s[48:49] op_sel_hi:[1,0,0]
	v_pk_add_f32 v[26:27], v[68:69], v[8:9]
	v_pk_add_f32 v[24:25], v[24:25], 1.0 op_sel_hi:[1,0]
	v_med3_f32 v26, v26, s23, v243
	v_rcp_f32_e32 v24, v24
	v_rcp_f32_e32 v25, v25
	v_med3_f32 v27, v27, s23, v243
	v_pk_fma_f32 v[26:27], v[26:27], s[48:49], s[48:49] op_sel_hi:[1,0,0]
	v_pk_add_f32 v[6:7], v[58:59], v[6:7]
	v_pk_mul_f32 v[12:13], v[12:13], v[24:25]
	v_med3_f32 v6, v6, s23, v243
	v_pk_mul_f32 v[24:25], v[28:29], v[12:13]
	v_pk_fma_f32 v[12:13], v[72:73], s[26:27], v[18:19] op_sel_hi:[1,0,1]
	v_med3_f32 v7, v7, s23, v243
	v_max_f32_e32 v12, 0xc1898193, v12
	v_max_f32_e32 v13, 0xc1898193, v13
	v_exp_f32_e32 v28, v12
	v_exp_f32_e32 v29, v13
	v_pk_fma_f32 v[18:19], v[64:65], s[26:27], v[18:19] op_sel_hi:[1,0,1]
	v_pk_fma_f32 v[6:7], v[6:7], s[48:49], s[48:49] op_sel_hi:[1,0,0]
	v_max_f32_e32 v18, 0xc1898193, v18
	v_pk_add_f32 v[28:29], v[28:29], 1.0 op_sel_hi:[1,0]
	v_max_f32_e32 v19, 0xc1898193, v19
	v_rcp_f32_e32 v28, v28
	v_rcp_f32_e32 v29, v29
	v_pk_add_f32 v[8:9], v[60:61], v[8:9]
	v_pk_mul_f32 v[12:13], v[12:13], v[28:29]
	s_nop 0
	v_pk_mul_f32 v[26:27], v[26:27], v[12:13]
	v_mov_b32_e32 v12, v1
	v_cvt_pk_fp8_f32 v12, v24, v25
	v_exp_f32_e32 v24, v20
	v_exp_f32_e32 v25, v21
	v_mov_b32_e32 v13, v1
	v_med3_f32 v8, v8, s23, v243
	v_med3_f32 v9, v9, s23, v243
	v_pk_add_f32 v[24:25], v[24:25], 1.0 op_sel_hi:[1,0]
	v_pk_fma_f32 v[8:9], v[8:9], s[48:49], s[48:49] op_sel_hi:[1,0,0]
	v_rcp_f32_e32 v24, v24
	v_rcp_f32_e32 v25, v25
	v_cvt_pk_fp8_f32 v12, v26, v27 op_sel:[0,0,1]
	v_pk_mul_f32 v[20:21], v[20:21], v[24:25]
	s_nop 0
	v_pk_mul_f32 v[6:7], v[6:7], v[20:21]
	v_exp_f32_e32 v20, v18
	v_exp_f32_e32 v21, v19
	v_cvt_pk_fp8_f32 v13, v6, v7
	v_lshl_add_u64 v[6:7], s[12:13], 0, v[22:23]
	v_permlane32_swap_b32_e32 v10, v12
	v_pk_add_f32 v[20:21], v[20:21], 1.0 op_sel_hi:[1,0]
	s_nop 0
	v_rcp_f32_e32 v20, v20
	v_rcp_f32_e32 v21, v21
	s_nop 0
	v_pk_mul_f32 v[18:19], v[18:19], v[20:21]
	s_nop 0
	v_pk_mul_f32 v[8:9], v[8:9], v[18:19]
	v_lshl_add_u64 v[18:19], v[6:7], 0, s[4:5]
	v_pk_fma_f32 v[6:7], v[54:55], s[26:27], v[16:17] op_sel_hi:[1,0,1]
	v_cvt_pk_fp8_f32 v13, v8, v9 op_sel:[0,0,1]
	v_max_f32_e32 v6, 0xc1898193, v6
	v_max_f32_e32 v7, 0xc1898193, v7
	v_exp_f32_e32 v8, v6
	v_exp_f32_e32 v9, v7
	v_permlane32_swap_b32_e32 v11, v13
	s_nop 1
	v_permlane16_swap_b32_e32 v10, v11
	v_pk_add_f32 v[8:9], v[8:9], 1.0 op_sel_hi:[1,0]
	v_permlane16_swap_b32_e32 v12, v13
	v_rcp_f32_e32 v8, v8
	v_rcp_f32_e32 v9, v9
	global_store_dwordx4 v[18:19], v[10:13], off
	v_pk_add_f32 v[20:21], v[42:43], v[2:3]
	s_mov_b64 s[4:5], -1
	v_pk_add_f32 v[12:13], v[50:51], v[2:3]
	v_pk_mul_f32 v[6:7], v[6:7], v[8:9]
	v_med3_f32 v12, v12, s23, v243
	v_med3_f32 v13, v13, s23, v243
	v_pk_fma_f32 v[12:13], v[12:13], s[48:49], s[48:49] op_sel_hi:[1,0,0]
	v_pk_add_f32 v[10:11], v[52:53], v[4:5]
	v_pk_mul_f32 v[8:9], v[12:13], v[6:7]
	v_pk_fma_f32 v[6:7], v[56:57], s[26:27], v[14:15] op_sel_hi:[1,0,1]
	v_med3_f32 v10, v10, s23, v243
	v_max_f32_e32 v6, 0xc1898193, v6
	v_max_f32_e32 v7, 0xc1898193, v7
	v_exp_f32_e32 v12, v6
	v_exp_f32_e32 v13, v7
	v_med3_f32 v11, v11, s23, v243
	v_pk_fma_f32 v[10:11], v[10:11], s[48:49], s[48:49] op_sel_hi:[1,0,0]
	v_med3_f32 v20, v20, s23, v243
	v_pk_add_f32 v[12:13], v[12:13], 1.0 op_sel_hi:[1,0]
	v_med3_f32 v21, v21, s23, v243
	v_rcp_f32_e32 v12, v12
	v_rcp_f32_e32 v13, v13
	v_pk_fma_f32 v[20:21], v[20:21], s[48:49], s[48:49] op_sel_hi:[1,0,0]
	v_pk_mul_f32 v[6:7], v[6:7], v[12:13]
	s_nop 0
	v_pk_mul_f32 v[10:11], v[10:11], v[6:7]
	v_mov_b32_e32 v6, v1
	v_cvt_pk_fp8_f32 v6, v8, v9
	v_pk_fma_f32 v[8:9], v[46:47], s[26:27], v[16:17] op_sel_hi:[1,0,1]
	v_mov_b32_e32 v7, v1
	v_max_f32_e32 v8, 0xc1898193, v8
	v_max_f32_e32 v9, 0xc1898193, v9
	v_cvt_pk_fp8_f32 v6, v10, v11 op_sel:[0,0,1]
	v_exp_f32_e32 v10, v8
	v_exp_f32_e32 v11, v9
	v_pk_add_f32 v[12:13], v[44:45], v[4:5]
	v_pk_add_f32 v[10:11], v[10:11], 1.0 op_sel_hi:[1,0]
	s_nop 0
	v_rcp_f32_e32 v10, v10
	v_rcp_f32_e32 v11, v11
	v_med3_f32 v12, v12, s23, v243
	v_med3_f32 v13, v13, s23, v243
	v_pk_fma_f32 v[12:13], v[12:13], s[48:49], s[48:49] op_sel_hi:[1,0,0]
	v_pk_mul_f32 v[8:9], v[8:9], v[10:11]
	v_pk_fma_f32 v[10:11], v[48:49], s[26:27], v[14:15] op_sel_hi:[1,0,1]
	v_pk_mul_f32 v[8:9], v[20:21], v[8:9]
	v_max_f32_e32 v10, 0xc1898193, v10
	v_max_f32_e32 v11, 0xc1898193, v11
	v_exp_f32_e32 v20, v10
	v_exp_f32_e32 v21, v11
	v_cvt_pk_fp8_f32 v7, v8, v9
	v_pk_fma_f32 v[8:9], v[38:39], s[26:27], v[16:17] op_sel_hi:[1,0,1]
	v_pk_add_f32 v[20:21], v[20:21], 1.0 op_sel_hi:[1,0]
	s_nop 0
	v_rcp_f32_e32 v20, v20
	v_rcp_f32_e32 v21, v21
	v_max_f32_e32 v8, 0xc1898193, v8
	v_max_f32_e32 v9, 0xc1898193, v9
	v_pk_mul_f32 v[10:11], v[10:11], v[20:21]
	s_nop 0
	v_pk_mul_f32 v[10:11], v[12:13], v[10:11]
	v_pk_add_f32 v[20:21], v[34:35], v[2:3]
	v_cvt_pk_fp8_f32 v7, v10, v11 op_sel:[0,0,1]
	v_exp_f32_e32 v10, v8
	v_exp_f32_e32 v11, v9
	v_med3_f32 v20, v20, s23, v243
	v_med3_f32 v21, v21, s23, v243
	v_pk_fma_f32 v[20:21], v[20:21], s[48:49], s[48:49] op_sel_hi:[1,0,0]
	v_pk_add_f32 v[10:11], v[10:11], 1.0 op_sel_hi:[1,0]
	v_pk_add_f32 v[12:13], v[36:37], v[4:5]
	v_rcp_f32_e32 v10, v10
	v_rcp_f32_e32 v11, v11
	v_med3_f32 v12, v12, s23, v243
	v_med3_f32 v13, v13, s23, v243
	v_pk_fma_f32 v[12:13], v[12:13], s[48:49], s[48:49] op_sel_hi:[1,0,0]
	v_pk_mul_f32 v[8:9], v[8:9], v[10:11]
	v_pk_add_f32 v[2:3], v[158:159], v[2:3]
	v_pk_mul_f32 v[10:11], v[20:21], v[8:9]
	v_pk_fma_f32 v[8:9], v[40:41], s[26:27], v[14:15] op_sel_hi:[1,0,1]
	v_med3_f32 v2, v2, s23, v243
	v_max_f32_e32 v8, 0xc1898193, v8
	v_max_f32_e32 v9, 0xc1898193, v9
	v_exp_f32_e32 v20, v8
	v_exp_f32_e32 v21, v9
	v_med3_f32 v3, v3, s23, v243
	v_pk_fma_f32 v[2:3], v[2:3], s[48:49], s[48:49] op_sel_hi:[1,0,0]
	v_pk_add_f32 v[4:5], v[160:161], v[4:5]
	v_pk_add_f32 v[20:21], v[20:21], 1.0 op_sel_hi:[1,0]
	v_med3_f32 v4, v4, s23, v243
	v_rcp_f32_e32 v20, v20
	v_rcp_f32_e32 v21, v21
	v_med3_f32 v5, v5, s23, v243
	v_pk_fma_f32 v[4:5], v[4:5], s[48:49], s[48:49] op_sel_hi:[1,0,0]
	v_pk_mul_f32 v[8:9], v[8:9], v[20:21]
	s_nop 0
	v_pk_mul_f32 v[12:13], v[12:13], v[8:9]
	v_mov_b32_e32 v8, v1
	v_cvt_pk_fp8_f32 v8, v10, v11
	v_pk_fma_f32 v[10:11], v[154:155], s[26:27], v[16:17] op_sel_hi:[1,0,1]
	v_mov_b32_e32 v9, v1
	v_max_f32_e32 v10, 0xc1898193, v10
	v_max_f32_e32 v11, 0xc1898193, v11
	v_cvt_pk_fp8_f32 v8, v12, v13 op_sel:[0,0,1]
	v_exp_f32_e32 v12, v10
	v_exp_f32_e32 v13, v11
	v_permlane32_swap_b32_e32 v6, v8
	v_pk_add_f32 v[12:13], v[12:13], 1.0 op_sel_hi:[1,0]
	s_nop 0
	v_rcp_f32_e32 v12, v12
	v_rcp_f32_e32 v13, v13
	s_nop 0
	v_pk_mul_f32 v[10:11], v[10:11], v[12:13]
	s_nop 0
	v_pk_mul_f32 v[2:3], v[2:3], v[10:11]
	v_pk_fma_f32 v[10:11], v[156:157], s[26:27], v[14:15] op_sel_hi:[1,0,1]
	v_cvt_pk_fp8_f32 v9, v2, v3
	v_max_f32_e32 v10, 0xc1898193, v10
	v_max_f32_e32 v11, 0xc1898193, v11
	v_exp_f32_e32 v12, v10
	v_exp_f32_e32 v13, v11
	s_nop 0
	v_pk_add_f32 v[12:13], v[12:13], 1.0 op_sel_hi:[1,0]
	s_nop 0
	v_rcp_f32_e32 v12, v12
	v_rcp_f32_e32 v13, v13
	s_nop 0
	v_pk_mul_f32 v[10:11], v[10:11], v[12:13]
	s_nop 0
	v_pk_mul_f32 v[4:5], v[4:5], v[10:11]
	s_nop 0
	v_cvt_pk_fp8_f32 v9, v4, v5 op_sel:[0,0,1]
	s_nop 1
	v_permlane32_swap_b32_e32 v7, v9
	s_nop 1
	v_permlane16_swap_b32_e32 v6, v7
	v_permlane16_swap_b32_e32 v8, v9
	global_store_dwordx4 v[18:19], v[6:9], off offset:64
	s_cbranch_vccnz .LBB0_1986
	v_readlane_b32 s0, v254, 61
	v_readlane_b32 s1, v254, 62
	s_andn2_b64 vcc, exec, s[0:1]
	s_cbranch_vccnz .LBB0_1985
	s_barrier
	s_branch .LBB0_1985

.LBB0_2092:
	s_lshl_b32 s13, s26, 10
	v_mbcnt_lo_u32_b32 v6, -1, 0
	v_mbcnt_hi_u32_b32 v6, -1, v6
	s_and_b32 s13, s13, 0x400
	v_ashrrev_i32_e32 v2, 1, v6
	v_and_b32_e32 v27, -8, v2
	s_add_i32 s13, s5, s13
	v_lshl_add_u32 v12, v27, 2, s13
	ds_read_b128 v[2:5], v12
	ds_read_b128 v[8:11], v12 offset:16
	ds_read_b128 v[18:21], v12 offset:512
	ds_read_b128 v[22:25], v12 offset:528
	s_lshl_b32 s13, s40, 8
	s_add_i32 s13, s13, s63
	s_waitcnt lgkmcnt(0)
	v_pk_mul_f32 v[14:15], v[2:3], s[22:23] op_sel_hi:[1,0]
	v_pk_mul_f32 v[16:17], v[8:9], s[22:23] op_sel_hi:[1,0]
	v_and_or_b32 v26, v6, 15, s13
	v_pk_mul_f32 v[6:7], v[4:5], s[22:23] op_sel_hi:[1,0]
	v_pk_mul_f32 v[12:13], v[10:11], s[22:23] op_sel_hi:[1,0]
	v_pk_mul_f32 v[4:5], v[24:25], s[22:23] op_sel_hi:[1,0]
	v_pk_mul_f32 v[10:11], v[22:23], s[22:23] op_sel_hi:[1,0]
	v_pk_fma_f32 v[22:23], v[158:159], s[22:23], v[14:15] op_sel_hi:[1,0,1]
	v_pk_fma_f32 v[24:25], v[154:155], s[22:23], v[16:17] op_sel_hi:[1,0,1]
	v_mov_b32_e32 v28, v1
	v_mov_b32_e32 v29, v1
	v_cvt_pk_fp8_f32 v28, v22, v23
	v_cvt_pk_fp8_f32 v29, v24, v25
	v_pk_mul_f32 v[8:9], v[18:19], s[22:23] op_sel_hi:[1,0]
	v_pk_fma_f32 v[22:23], v[160:161], s[22:23], v[6:7] op_sel_hi:[1,0,1]
	v_pk_fma_f32 v[24:25], v[156:157], s[22:23], v[12:13] op_sel_hi:[1,0,1]
	v_cvt_pk_fp8_f32 v28, v22, v23 op_sel:[0,0,1]
	v_cvt_pk_fp8_f32 v29, v24, v25 op_sel:[0,0,1]
	v_pk_fma_f32 v[22:23], v[126:127], s[22:23], v[8:9] op_sel_hi:[1,0,1]
	v_pk_fma_f32 v[24:25], v[122:123], s[22:23], v[10:11] op_sel_hi:[1,0,1]
	v_mov_b32_e32 v30, v1
	v_mov_b32_e32 v31, v1
	v_cvt_pk_fp8_f32 v30, v22, v23
	v_cvt_pk_fp8_f32 v31, v24, v25
	s_lshl_b32 s13, s36, 8
	v_pk_mul_f32 v[2:3], v[20:21], s[22:23] op_sel_hi:[1,0]
	s_or_b32 s13, s13, s64
	v_add_u32_e32 v20, s13, v27
	v_ashrrev_i32_e32 v27, 31, v26
	v_pk_fma_f32 v[22:23], v[128:129], s[22:23], v[2:3] op_sel_hi:[1,0,1]
	v_pk_fma_f32 v[24:25], v[124:125], s[22:23], v[4:5] op_sel_hi:[1,0,1]
	v_lshlrev_b64 v[18:19], 10, v[26:27]
	v_cvt_pk_fp8_f32 v30, v22, v23 op_sel:[0,0,1]
	v_cvt_pk_fp8_f32 v31, v24, v25 op_sel:[0,0,1]
	v_ashrrev_i32_e32 v21, 31, v20
	v_lshl_add_u64 v[18:19], s[6:7], 0, v[18:19]
	v_lshl_add_u64 v[18:19], v[18:19], 0, v[20:21]
	global_store_dwordx2 v[18:19], v[28:29], off
	global_store_dwordx2 v[18:19], v[30:31], off offset:128
	v_pk_fma_f32 v[24:25], v[150:151], s[22:23], v[14:15] op_sel_hi:[1,0,1]
	v_pk_fma_f32 v[28:29], v[146:147], s[22:23], v[16:17] op_sel_hi:[1,0,1]
	v_mov_b32_e32 v30, v1
	v_mov_b32_e32 v31, v1
	v_cvt_pk_fp8_f32 v30, v24, v25
	v_cvt_pk_fp8_f32 v31, v28, v29
	v_pk_fma_f32 v[24:25], v[152:153], s[22:23], v[6:7] op_sel_hi:[1,0,1]
	v_pk_fma_f32 v[28:29], v[148:149], s[22:23], v[12:13] op_sel_hi:[1,0,1]
	v_cvt_pk_fp8_f32 v30, v24, v25 op_sel:[0,0,1]
	v_cvt_pk_fp8_f32 v31, v28, v29 op_sel:[0,0,1]
	v_pk_fma_f32 v[24:25], v[118:119], s[22:23], v[8:9] op_sel_hi:[1,0,1]
	v_pk_fma_f32 v[28:29], v[114:115], s[22:23], v[10:11] op_sel_hi:[1,0,1]
	v_mov_b32_e32 v32, v1
	v_mov_b32_e32 v33, v1
	v_cvt_pk_fp8_f32 v32, v24, v25
	v_cvt_pk_fp8_f32 v33, v28, v29
	v_or_b32_e32 v22, 16, v26
	v_ashrrev_i32_e32 v23, 31, v22
	v_pk_fma_f32 v[24:25], v[120:121], s[22:23], v[2:3] op_sel_hi:[1,0,1]
	v_pk_fma_f32 v[28:29], v[116:117], s[22:23], v[4:5] op_sel_hi:[1,0,1]
	v_lshlrev_b64 v[22:23], 10, v[22:23]
	v_cvt_pk_fp8_f32 v32, v24, v25 op_sel:[0,0,1]
	v_cvt_pk_fp8_f32 v33, v28, v29 op_sel:[0,0,1]
	v_lshl_add_u64 v[22:23], s[6:7], 0, v[22:23]
	v_lshl_add_u64 v[22:23], v[22:23], 0, v[20:21]
	global_store_dwordx2 v[22:23], v[30:31], off
	global_store_dwordx2 v[22:23], v[32:33], off offset:128
	v_pk_fma_f32 v[24:25], v[142:143], s[22:23], v[14:15] op_sel_hi:[1,0,1]
	v_pk_fma_f32 v[28:29], v[138:139], s[22:23], v[16:17] op_sel_hi:[1,0,1]
	v_mov_b32_e32 v30, v1
	v_mov_b32_e32 v31, v1
	v_cvt_pk_fp8_f32 v30, v24, v25
	v_cvt_pk_fp8_f32 v31, v28, v29
	v_pk_fma_f32 v[24:25], v[144:145], s[22:23], v[6:7] op_sel_hi:[1,0,1]
	v_pk_fma_f32 v[28:29], v[140:141], s[22:23], v[12:13] op_sel_hi:[1,0,1]
	v_cvt_pk_fp8_f32 v30, v24, v25 op_sel:[0,0,1]
	v_cvt_pk_fp8_f32 v31, v28, v29 op_sel:[0,0,1]
	v_pk_fma_f32 v[24:25], v[110:111], s[22:23], v[8:9] op_sel_hi:[1,0,1]
	v_pk_fma_f32 v[28:29], v[106:107], s[22:23], v[10:11] op_sel_hi:[1,0,1]
	v_mov_b32_e32 v32, v1
	v_mov_b32_e32 v33, v1
	v_cvt_pk_fp8_f32 v32, v24, v25
	v_cvt_pk_fp8_f32 v33, v28, v29
	v_or_b32_e32 v22, 32, v26
	v_ashrrev_i32_e32 v23, 31, v22
	v_pk_fma_f32 v[24:25], v[112:113], s[22:23], v[2:3] op_sel_hi:[1,0,1]
	v_pk_fma_f32 v[28:29], v[108:109], s[22:23], v[4:5] op_sel_hi:[1,0,1]
	v_lshlrev_b64 v[22:23], 10, v[22:23]
	v_cvt_pk_fp8_f32 v32, v24, v25 op_sel:[0,0,1]
	v_cvt_pk_fp8_f32 v33, v28, v29 op_sel:[0,0,1]
	v_lshl_add_u64 v[22:23], s[6:7], 0, v[22:23]
	v_lshl_add_u64 v[22:23], v[22:23], 0, v[20:21]
	global_store_dwordx2 v[22:23], v[30:31], off
	global_store_dwordx2 v[22:23], v[32:33], off offset:128
	v_or_b32_e32 v22, 48, v26
	v_pk_fma_f32 v[24:25], v[134:135], s[22:23], v[14:15] op_sel_hi:[1,0,1]
	v_pk_fma_f32 v[26:27], v[130:131], s[22:23], v[16:17] op_sel_hi:[1,0,1]
	v_mov_b32_e32 v28, v1
	v_mov_b32_e32 v29, v1
	v_cvt_pk_fp8_f32 v28, v24, v25
	v_cvt_pk_fp8_f32 v29, v26, v27
	v_pk_fma_f32 v[24:25], v[136:137], s[22:23], v[6:7] op_sel_hi:[1,0,1]
	v_pk_fma_f32 v[26:27], v[132:133], s[22:23], v[12:13] op_sel_hi:[1,0,1]
	v_cvt_pk_fp8_f32 v28, v24, v25 op_sel:[0,0,1]
	v_cvt_pk_fp8_f32 v29, v26, v27 op_sel:[0,0,1]
	v_pk_fma_f32 v[24:25], v[102:103], s[22:23], v[8:9] op_sel_hi:[1,0,1]
	v_pk_fma_f32 v[26:27], v[98:99], s[22:23], v[10:11] op_sel_hi:[1,0,1]
	v_mov_b32_e32 v30, v1
	v_mov_b32_e32 v31, v1
	v_cvt_pk_fp8_f32 v30, v24, v25
	v_cvt_pk_fp8_f32 v31, v26, v27
	v_ashrrev_i32_e32 v23, 31, v22
	v_lshlrev_b64 v[22:23], 10, v[22:23]
	v_pk_fma_f32 v[24:25], v[104:105], s[22:23], v[2:3] op_sel_hi:[1,0,1]
	v_pk_fma_f32 v[26:27], v[100:101], s[22:23], v[4:5] op_sel_hi:[1,0,1]
	v_lshl_add_u64 v[22:23], s[6:7], 0, v[22:23]
	v_cvt_pk_fp8_f32 v30, v24, v25 op_sel:[0,0,1]
	v_cvt_pk_fp8_f32 v31, v26, v27 op_sel:[0,0,1]
	v_lshl_add_u64 v[20:21], v[22:23], 0, v[20:21]
	v_pk_fma_f32 v[22:23], v[94:95], s[22:23], v[14:15] op_sel_hi:[1,0,1]
	v_pk_fma_f32 v[24:25], v[90:91], s[22:23], v[16:17] op_sel_hi:[1,0,1]
	v_mov_b32_e32 v26, v1
	v_mov_b32_e32 v27, v1
	v_cvt_pk_fp8_f32 v26, v22, v23
	v_cvt_pk_fp8_f32 v27, v24, v25
	v_pk_fma_f32 v[22:23], v[96:97], s[22:23], v[6:7] op_sel_hi:[1,0,1]
	v_pk_fma_f32 v[24:25], v[92:93], s[22:23], v[12:13] op_sel_hi:[1,0,1]
	global_store_dwordx2 v[20:21], v[28:29], off
	global_store_dwordx2 v[20:21], v[30:31], off offset:128
	v_cvt_pk_fp8_f32 v26, v22, v23 op_sel:[0,0,1]
	v_cvt_pk_fp8_f32 v27, v24, v25 op_sel:[0,0,1]
	v_pk_fma_f32 v[22:23], v[62:63], s[22:23], v[8:9] op_sel_hi:[1,0,1]
	v_pk_fma_f32 v[24:25], v[58:59], s[22:23], v[10:11] op_sel_hi:[1,0,1]
	v_mov_b32_e32 v28, v1
	v_mov_b32_e32 v29, v1
	v_cvt_pk_fp8_f32 v28, v22, v23
	v_cvt_pk_fp8_f32 v29, v24, v25
	v_pk_fma_f32 v[22:23], v[64:65], s[22:23], v[2:3] op_sel_hi:[1,0,1]
	v_pk_fma_f32 v[24:25], v[60:61], s[22:23], v[4:5] op_sel_hi:[1,0,1]
	v_cvt_pk_fp8_f32 v28, v22, v23 op_sel:[0,0,1]
	v_cvt_pk_fp8_f32 v29, v24, v25 op_sel:[0,0,1]
	s_mov_b32 s13, 0x20000
	v_add_co_u32_e32 v22, vcc, s13, v18
	s_mov_b64 s[26:27], 0x20000
	s_nop 0
	v_addc_co_u32_e32 v23, vcc, 0, v19, vcc
	v_lshl_add_u64 v[20:21], v[18:19], 0, s[26:27]
	global_store_dwordx2 v[22:23], v[26:27], off
	global_store_dwordx2 v[20:21], v[28:29], off offset:128
	v_pk_fma_f32 v[22:23], v[86:87], s[22:23], v[14:15] op_sel_hi:[1,0,1]
	v_pk_fma_f32 v[24:25], v[82:83], s[22:23], v[16:17] op_sel_hi:[1,0,1]
	v_mov_b32_e32 v26, v1
	v_mov_b32_e32 v27, v1
	v_cvt_pk_fp8_f32 v26, v22, v23
	v_cvt_pk_fp8_f32 v27, v24, v25
	v_pk_fma_f32 v[22:23], v[88:89], s[22:23], v[6:7] op_sel_hi:[1,0,1]
	v_pk_fma_f32 v[24:25], v[84:85], s[22:23], v[12:13] op_sel_hi:[1,0,1]
	v_cvt_pk_fp8_f32 v26, v22, v23 op_sel:[0,0,1]
	v_cvt_pk_fp8_f32 v27, v24, v25 op_sel:[0,0,1]
	v_pk_fma_f32 v[22:23], v[54:55], s[22:23], v[8:9] op_sel_hi:[1,0,1]
	v_pk_fma_f32 v[24:25], v[50:51], s[22:23], v[10:11] op_sel_hi:[1,0,1]
	v_mov_b32_e32 v28, v1
	v_mov_b32_e32 v29, v1
	v_cvt_pk_fp8_f32 v28, v22, v23
	v_cvt_pk_fp8_f32 v29, v24, v25
	v_pk_fma_f32 v[22:23], v[56:57], s[22:23], v[2:3] op_sel_hi:[1,0,1]
	v_pk_fma_f32 v[24:25], v[52:53], s[22:23], v[4:5] op_sel_hi:[1,0,1]
	v_cvt_pk_fp8_f32 v28, v22, v23 op_sel:[0,0,1]
	v_cvt_pk_fp8_f32 v29, v24, v25 op_sel:[0,0,1]
	s_mov_b32 s13, 0x24000
	v_add_co_u32_e32 v22, vcc, s13, v18
	s_mov_b64 s[26:27], 0x24000
	s_nop 0
	v_addc_co_u32_e32 v23, vcc, 0, v19, vcc
	v_lshl_add_u64 v[20:21], v[18:19], 0, s[26:27]
	global_store_dwordx2 v[22:23], v[26:27], off
	global_store_dwordx2 v[20:21], v[28:29], off offset:128
	v_pk_fma_f32 v[22:23], v[78:79], s[22:23], v[14:15] op_sel_hi:[1,0,1]
	v_pk_fma_f32 v[24:25], v[74:75], s[22:23], v[16:17] op_sel_hi:[1,0,1]
	v_mov_b32_e32 v26, v1
	v_mov_b32_e32 v27, v1
	v_cvt_pk_fp8_f32 v26, v22, v23
	v_cvt_pk_fp8_f32 v27, v24, v25
	v_pk_fma_f32 v[22:23], v[80:81], s[22:23], v[6:7] op_sel_hi:[1,0,1]
	v_pk_fma_f32 v[24:25], v[76:77], s[22:23], v[12:13] op_sel_hi:[1,0,1]
	v_cvt_pk_fp8_f32 v26, v22, v23 op_sel:[0,0,1]
	v_cvt_pk_fp8_f32 v27, v24, v25 op_sel:[0,0,1]
	v_pk_fma_f32 v[22:23], v[46:47], s[22:23], v[8:9] op_sel_hi:[1,0,1]
	v_pk_fma_f32 v[24:25], v[42:43], s[22:23], v[10:11] op_sel_hi:[1,0,1]
	v_mov_b32_e32 v28, v1
	v_mov_b32_e32 v29, v1
	v_cvt_pk_fp8_f32 v28, v22, v23
	v_cvt_pk_fp8_f32 v29, v24, v25
	v_pk_fma_f32 v[22:23], v[48:49], s[22:23], v[2:3] op_sel_hi:[1,0,1]
	v_pk_fma_f32 v[24:25], v[44:45], s[22:23], v[4:5] op_sel_hi:[1,0,1]
	v_cvt_pk_fp8_f32 v28, v22, v23 op_sel:[0,0,1]
	v_cvt_pk_fp8_f32 v29, v24, v25 op_sel:[0,0,1]
	s_mov_b32 s13, 0x28000
	v_add_co_u32_e32 v22, vcc, s13, v18
	s_mov_b64 s[26:27], 0x28000
	s_nop 0
	v_addc_co_u32_e32 v23, vcc, 0, v19, vcc
	v_lshl_add_u64 v[20:21], v[18:19], 0, s[26:27]
	global_store_dwordx2 v[22:23], v[26:27], off
	global_store_dwordx2 v[20:21], v[28:29], off offset:128
	v_pk_fma_f32 v[14:15], v[70:71], s[22:23], v[14:15] op_sel_hi:[1,0,1]
	v_mov_b32_e32 v22, v1
	v_cvt_pk_fp8_f32 v22, v14, v15
	v_pk_fma_f32 v[16:17], v[66:67], s[22:23], v[16:17] op_sel_hi:[1,0,1]
	v_mov_b32_e32 v23, v1
	v_pk_fma_f32 v[6:7], v[72:73], s[22:23], v[6:7] op_sel_hi:[1,0,1]
	v_cvt_pk_fp8_f32 v23, v16, v17
	v_cvt_pk_fp8_f32 v22, v6, v7 op_sel:[0,0,1]
	v_pk_fma_f32 v[6:7], v[38:39], s[22:23], v[8:9] op_sel_hi:[1,0,1]
	v_pk_fma_f32 v[8:9], v[34:35], s[22:23], v[10:11] op_sel_hi:[1,0,1]
	v_mov_b32_e32 v10, v1
	v_mov_b32_e32 v11, v1
	v_cvt_pk_fp8_f32 v10, v6, v7
	v_cvt_pk_fp8_f32 v11, v8, v9
	v_pk_fma_f32 v[12:13], v[68:69], s[22:23], v[12:13] op_sel_hi:[1,0,1]
	v_pk_fma_f32 v[2:3], v[40:41], s[22:23], v[2:3] op_sel_hi:[1,0,1]
	v_cvt_pk_fp8_f32 v23, v12, v13 op_sel:[0,0,1]
	v_pk_fma_f32 v[4:5], v[36:37], s[22:23], v[4:5] op_sel_hi:[1,0,1]
	s_mov_b32 s13, 0x2c000
	v_cvt_pk_fp8_f32 v10, v2, v3 op_sel:[0,0,1]
	v_cvt_pk_fp8_f32 v11, v4, v5 op_sel:[0,0,1]
	v_add_co_u32_e32 v2, vcc, s13, v18
	s_mov_b64 s[26:27], 0x2c000
	s_nop 0
	v_addc_co_u32_e32 v3, vcc, 0, v19, vcc
	s_and_b64 vcc, exec, s[0:1]
	s_mov_b64 s[0:1], -1
	v_lshl_add_u64 v[20:21], v[18:19], 0, s[26:27]
	global_store_dwordx2 v[2:3], v[22:23], off
	global_store_dwordx2 v[20:21], v[10:11], off offset:128
	s_cbranch_vccnz .LBB0_2075
	v_readlane_b32 s0, v254, 40
	v_readlane_b32 s1, v254, 41
	s_andn2_b64 vcc, exec, s[0:1]
	s_cbranch_vccnz .LBB0_2074
	s_barrier
	s_branch .LBB0_2074

.LBB0_2186:
	v_readlane_b32 s4, v252, 15
	v_readlane_b32 s5, v252, 16
	v_cvt_f32_u32_e32 v0, v3
	v_sub_u32_e32 v5, 0, v3
	v_rcp_iflag_f32_e32 v0, v0
	s_nop 1
	global_atomic_add v4, v1, v236, s[4:5] sc0
	v_mul_f32_e32 v0, 0x4f7ffffe, v0
	v_cvt_u32_f32_e32 v0, v0
	v_mul_lo_u32 v5, v5, v0
	v_mul_hi_u32 v5, v0, v5
	v_add_u32_e32 v0, v0, v5
	s_waitcnt vmcnt(0)
	v_mul_hi_u32 v0, v4, v0
	v_mul_lo_u32 v5, v0, v3
	v_sub_u32_e32 v5, v4, v5
	v_add_u32_e32 v6, 1, v0
	v_cmp_ge_u32_e32 vcc, v5, v3
	v_add_u32_e32 v4, 1, v4
	s_nop 0
	v_cndmask_b32_e32 v0, v0, v6, vcc
	v_sub_u32_e32 v6, v5, v3
	v_cndmask_b32_e32 v5, v5, v6, vcc
	v_add_u32_e32 v6, 1, v0
	v_cmp_ge_u32_e32 vcc, v5, v3
	s_nop 1
	v_cndmask_b32_e32 v0, v0, v6, vcc
	v_mul_lo_u32 v5, v3, v0
	v_add_u32_e32 v3, v5, v3
	v_cmp_ne_u32_e32 vcc, v4, v3
	s_and_saveexec_b64 s[4:5], vcc
	s_xor_b64 s[4:5], exec, s[4:5]
	s_cbranch_execz .LBB0_2200
	v_readlane_b32 s6, v252, 21
	v_readlane_b32 s7, v252, 22
	s_waitcnt lgkmcnt(0)
	s_nop 3
	global_load_dword v2, v1, s[6:7] sc1
	s_waitcnt vmcnt(0)
	v_cmp_eq_u32_e32 vcc, v2, v0
	s_and_saveexec_b64 s[6:7], vcc
	s_cbranch_execz .LBB0_2199
	s_mov_b32 s23, 1
	s_mov_b64 s[8:9], 0
	s_branch .LBB0_2190
